# in-proj sigmoid-gate epilogue rewritten by hand (5 VALU per element: 1/255 folded into the rcp argument, v_cvt_rpi + SDWA byte insert) on top of the SwiGLU epilogue rewrite; f32 math, u8 gates as base
# speedup vs baseline: 1.0109x; 1.0076x over previous
;     __device__ __forceinline__ void operator()(const f32x4 (&acc)[2][2][4][2], const Unit& u, int wr, int wc, int fr, int fq) const {
;     ...
;                 unsigned char* gb8 = wsb + (pn < 14 ? WS_GA : WS_GB) + ((pn - 10) & 3) * 256 + cl;
; #pragma unroll
;                 for (int ai = 0; ai < 2; ++ai)
; #pragma unroll
;                     for (int m = 0; m < 4; ++m) { unsigned char* rowp = gb8 + (size_t)(row0 + ai * HALF + m * 16) * 1024; const float nrf = -1.4426950408889634f * rsr[ai * HALF + m * 16];
; #pragma unroll
;                         for (int bj = 0; bj < 2; ++bj) { u32x2 w; w.x = 0u; w.y = 0u;
; #pragma unroll
;                             for (int e = 0; e < 4; ++e) { const float x0 = acc[ai][bj][m][0][e], x1 = acc[ai][bj][m][1][e];
;                                 const float r0 = 255.0f * __builtin_amdgcn_rcpf(1.0f + __builtin_amdgcn_exp2f(nrf * x0)), r1 = 255.0f * __builtin_amdgcn_rcpf(1.0f + __builtin_amdgcn_exp2f(nrf * x1));
;                                 w.x |= (unsigned)(r0 + 0.5f) << (8 * e); w.y |= (unsigned)(r1 + 0.5f) << (8 * e); }
;                             *(u32x2*)(rowp + bj * HALF) = w; }
;                         asm volatile("" ::: "memory"); }
.LBB0_398:
	s_and_b32 s0, s70, -4
	v_lshl_add_u32 v132, s18, 8, v202
	s_cmp_lg_u32 s0, 4
	s_mov_b64 s[0:1], -1
	s_cbranch_scc0 .LBB0_538
	s_cmp_gt_i32 s70, 9
	s_cbranch_scc0 .LBB0_401
	ds_read_b32 v160, v205
	s_cmp_lt_u32 s70, 14
	s_brev_b32 s0, 8
	s_cselect_b32 s0, s0, 0x11000000
	s_add_u32 s0, s16, s0
	s_addc_u32 s1, s17, 0
	s_lshl_b32 s8, s70, 8
	s_and_b32 s8, s8, 0x300
	s_xor_b32 s8, s8, 0x200
	s_add_u32 s0, s0, s8
	s_addc_u32 s1, s1, 0
	v_ashrrev_i32_e32 v133, 31, v132
	v_lshlrev_b64 v[134:135], 10, v[132:133]
	v_lshl_add_u64 v[136:137], s[0:1], 0, v[172:173]
	v_lshl_add_u64 v[134:135], v[136:137], 0, v[134:135]
	s_mov_b32 s8, 0x3b808081
	s_waitcnt lgkmcnt(0)
	ds_read_b32 v161, v205 offset:64
	v_mul_f32_e32 v160, 0xbfb8aa3b, v160
	v_mul_f32_e32 v140, v160, v128
	v_mul_f32_e32 v141, v160, v129
	v_mul_f32_e32 v142, v160, v130
	v_mul_f32_e32 v143, v160, v131
	v_mul_f32_e32 v144, v160, v124
	v_mul_f32_e32 v145, v160, v125
	v_mul_f32_e32 v146, v160, v126
	v_mul_f32_e32 v147, v160, v127
	v_mul_f32_e32 v148, v160, v120
	v_mul_f32_e32 v149, v160, v121
	v_mul_f32_e32 v150, v160, v122
	v_mul_f32_e32 v151, v160, v123
	v_mul_f32_e32 v152, v160, v116
	v_mul_f32_e32 v153, v160, v117
	v_mul_f32_e32 v154, v160, v118
	v_mul_f32_e32 v155, v160, v119
	v_exp_f32_e32 v140, v140
	v_exp_f32_e32 v141, v141
	v_exp_f32_e32 v142, v142
	v_exp_f32_e32 v143, v143
	v_exp_f32_e32 v144, v144
	v_exp_f32_e32 v145, v145
	v_exp_f32_e32 v146, v146
	v_exp_f32_e32 v147, v147
	v_exp_f32_e32 v148, v148
	v_exp_f32_e32 v149, v149
	v_exp_f32_e32 v150, v150
	v_exp_f32_e32 v151, v151
	v_exp_f32_e32 v152, v152
	v_exp_f32_e32 v153, v153
	v_exp_f32_e32 v154, v154
	v_exp_f32_e32 v155, v155
	v_fma_f32 v140, v140, s8, s8
	v_fma_f32 v141, v141, s8, s8
	v_fma_f32 v142, v142, s8, s8
	v_fma_f32 v143, v143, s8, s8
	v_fma_f32 v144, v144, s8, s8
	v_fma_f32 v145, v145, s8, s8
	v_fma_f32 v146, v146, s8, s8
	v_fma_f32 v147, v147, s8, s8
	v_fma_f32 v148, v148, s8, s8
	v_fma_f32 v149, v149, s8, s8
	v_fma_f32 v150, v150, s8, s8
	v_fma_f32 v151, v151, s8, s8
	v_fma_f32 v152, v152, s8, s8
	v_fma_f32 v153, v153, s8, s8
	v_fma_f32 v154, v154, s8, s8
	v_fma_f32 v155, v155, s8, s8
	v_rcp_f32_e32 v140, v140
	v_rcp_f32_e32 v141, v141
	v_rcp_f32_e32 v142, v142
	v_rcp_f32_e32 v143, v143
	v_rcp_f32_e32 v144, v144
	v_rcp_f32_e32 v145, v145
	v_rcp_f32_e32 v146, v146
	v_rcp_f32_e32 v147, v147
	v_rcp_f32_e32 v148, v148
	v_rcp_f32_e32 v149, v149
	v_rcp_f32_e32 v150, v150
	v_rcp_f32_e32 v151, v151
	v_rcp_f32_e32 v152, v152
	v_rcp_f32_e32 v153, v153
	v_rcp_f32_e32 v154, v154
	v_rcp_f32_e32 v155, v155
	v_cvt_rpi_i32_f32_sdwa v156, v140 dst_sel:BYTE_0 dst_unused:UNUSED_PAD src0_sel:DWORD
	v_cvt_rpi_i32_f32_sdwa v157, v144 dst_sel:BYTE_0 dst_unused:UNUSED_PAD src0_sel:DWORD
	v_cvt_rpi_i32_f32_sdwa v158, v148 dst_sel:BYTE_0 dst_unused:UNUSED_PAD src0_sel:DWORD
	v_cvt_rpi_i32_f32_sdwa v159, v152 dst_sel:BYTE_0 dst_unused:UNUSED_PAD src0_sel:DWORD
	v_cvt_rpi_i32_f32_sdwa v156, v141 dst_sel:BYTE_1 dst_unused:UNUSED_PRESERVE src0_sel:DWORD
	v_cvt_rpi_i32_f32_sdwa v157, v145 dst_sel:BYTE_1 dst_unused:UNUSED_PRESERVE src0_sel:DWORD
	v_cvt_rpi_i32_f32_sdwa v158, v149 dst_sel:BYTE_1 dst_unused:UNUSED_PRESERVE src0_sel:DWORD
	v_cvt_rpi_i32_f32_sdwa v159, v153 dst_sel:BYTE_1 dst_unused:UNUSED_PRESERVE src0_sel:DWORD
	v_cvt_rpi_i32_f32_sdwa v156, v142 dst_sel:BYTE_2 dst_unused:UNUSED_PRESERVE src0_sel:DWORD
	v_cvt_rpi_i32_f32_sdwa v157, v146 dst_sel:BYTE_2 dst_unused:UNUSED_PRESERVE src0_sel:DWORD
	v_cvt_rpi_i32_f32_sdwa v158, v150 dst_sel:BYTE_2 dst_unused:UNUSED_PRESERVE src0_sel:DWORD
	v_cvt_rpi_i32_f32_sdwa v159, v154 dst_sel:BYTE_2 dst_unused:UNUSED_PRESERVE src0_sel:DWORD
	v_cvt_rpi_i32_f32_sdwa v156, v143 dst_sel:BYTE_3 dst_unused:UNUSED_PRESERVE src0_sel:DWORD
	v_cvt_rpi_i32_f32_sdwa v157, v147 dst_sel:BYTE_3 dst_unused:UNUSED_PRESERVE src0_sel:DWORD
	v_cvt_rpi_i32_f32_sdwa v158, v151 dst_sel:BYTE_3 dst_unused:UNUSED_PRESERVE src0_sel:DWORD
	v_cvt_rpi_i32_f32_sdwa v159, v155 dst_sel:BYTE_3 dst_unused:UNUSED_PRESERVE src0_sel:DWORD
	s_nop 0
	global_store_dwordx2 v[134:135], v[156:157], off
	global_store_dwordx2 v[134:135], v[158:159], off offset:128
	s_nop 1
	s_waitcnt lgkmcnt(0)
	v_mov_b32_e32 v160, v161
	ds_read_b32 v161, v205 offset:128
	v_mul_f32_e32 v160, 0xbfb8aa3b, v160
	v_mul_f32_e32 v140, v160, v112
	v_mul_f32_e32 v141, v160, v113
	v_mul_f32_e32 v142, v160, v114
	v_mul_f32_e32 v143, v160, v115
	v_mul_f32_e32 v144, v160, v108
	v_mul_f32_e32 v145, v160, v109
	v_mul_f32_e32 v146, v160, v110
	v_mul_f32_e32 v147, v160, v111
	v_mul_f32_e32 v148, v160, v104
	v_mul_f32_e32 v149, v160, v105
	v_mul_f32_e32 v150, v160, v106
	v_mul_f32_e32 v151, v160, v107
	v_mul_f32_e32 v152, v160, v100
	v_mul_f32_e32 v153, v160, v101
	v_mul_f32_e32 v154, v160, v102
	v_mul_f32_e32 v155, v160, v103
	v_exp_f32_e32 v140, v140
	v_exp_f32_e32 v141, v141
	v_exp_f32_e32 v142, v142
	v_exp_f32_e32 v143, v143
	v_exp_f32_e32 v144, v144
	v_exp_f32_e32 v145, v145
	v_exp_f32_e32 v146, v146
	v_exp_f32_e32 v147, v147
	v_exp_f32_e32 v148, v148
	v_exp_f32_e32 v149, v149
	v_exp_f32_e32 v150, v150
	v_exp_f32_e32 v151, v151
	v_exp_f32_e32 v152, v152
	v_exp_f32_e32 v153, v153
	v_exp_f32_e32 v154, v154
	v_exp_f32_e32 v155, v155
	v_fma_f32 v140, v140, s8, s8
	v_fma_f32 v141, v141, s8, s8
	v_fma_f32 v142, v142, s8, s8
	v_fma_f32 v143, v143, s8, s8
	v_fma_f32 v144, v144, s8, s8
	v_fma_f32 v145, v145, s8, s8
	v_fma_f32 v146, v146, s8, s8
	v_fma_f32 v147, v147, s8, s8
	v_fma_f32 v148, v148, s8, s8
	v_fma_f32 v149, v149, s8, s8
	v_fma_f32 v150, v150, s8, s8
	v_fma_f32 v151, v151, s8, s8
	v_fma_f32 v152, v152, s8, s8
	v_fma_f32 v153, v153, s8, s8
	v_fma_f32 v154, v154, s8, s8
;     __device__ __forceinline__ void operator()(const f32x4 (&acc)[2][2][4][2], const Unit& u, int wr, int wc, int fr, int fq) const {
;     ...
;                 unsigned char* gb8 = wsb + (pn < 14 ? WS_GA : WS_GB) + ((pn - 10) & 3) * 256 + cl;
; #pragma unroll
;                 for (int ai = 0; ai < 2; ++ai)
; #pragma unroll
;                     for (int m = 0; m < 4; ++m) { unsigned char* rowp = gb8 + (size_t)(row0 + ai * HALF + m * 16) * 1024; const float nrf = -1.4426950408889634f * rsr[ai * HALF + m * 16];
; #pragma unroll
;                         for (int bj = 0; bj < 2; ++bj) { u32x2 w; w.x = 0u; w.y = 0u;
; #pragma unroll
;                             for (int e = 0; e < 4; ++e) { const float x0 = acc[ai][bj][m][0][e], x1 = acc[ai][bj][m][1][e];
;                                 const float r0 = 255.0f * __builtin_amdgcn_rcpf(1.0f + __builtin_amdgcn_exp2f(nrf * x0)), r1 = 255.0f * __builtin_amdgcn_rcpf(1.0f + __builtin_amdgcn_exp2f(nrf * x1));
;                                 w.x |= (unsigned)(r0 + 0.5f) << (8 * e); w.y |= (unsigned)(r1 + 0.5f) << (8 * e); }
;                             *(u32x2*)(rowp + bj * HALF) = w; }
;                         asm volatile("" ::: "memory"); }
	v_fma_f32 v155, v155, s8, s8
	v_rcp_f32_e32 v140, v140
	v_rcp_f32_e32 v141, v141
	v_rcp_f32_e32 v142, v142
	v_rcp_f32_e32 v143, v143
	v_rcp_f32_e32 v144, v144
	v_rcp_f32_e32 v145, v145
	v_rcp_f32_e32 v146, v146
	v_rcp_f32_e32 v147, v147
	v_rcp_f32_e32 v148, v148
	v_rcp_f32_e32 v149, v149
	v_rcp_f32_e32 v150, v150
	v_rcp_f32_e32 v151, v151
	v_rcp_f32_e32 v152, v152
	v_rcp_f32_e32 v153, v153
	v_rcp_f32_e32 v154, v154
	v_rcp_f32_e32 v155, v155
	s_mov_b64 s[0:1], 0x4000
	v_lshl_add_u64 v[136:137], v[134:135], 0, s[0:1]
	v_cvt_rpi_i32_f32_sdwa v156, v140 dst_sel:BYTE_0 dst_unused:UNUSED_PAD src0_sel:DWORD
	v_cvt_rpi_i32_f32_sdwa v157, v144 dst_sel:BYTE_0 dst_unused:UNUSED_PAD src0_sel:DWORD
	v_cvt_rpi_i32_f32_sdwa v158, v148 dst_sel:BYTE_0 dst_unused:UNUSED_PAD src0_sel:DWORD
	v_cvt_rpi_i32_f32_sdwa v159, v152 dst_sel:BYTE_0 dst_unused:UNUSED_PAD src0_sel:DWORD
	v_cvt_rpi_i32_f32_sdwa v156, v141 dst_sel:BYTE_1 dst_unused:UNUSED_PRESERVE src0_sel:DWORD
	v_cvt_rpi_i32_f32_sdwa v157, v145 dst_sel:BYTE_1 dst_unused:UNUSED_PRESERVE src0_sel:DWORD
	v_cvt_rpi_i32_f32_sdwa v158, v149 dst_sel:BYTE_1 dst_unused:UNUSED_PRESERVE src0_sel:DWORD
	v_cvt_rpi_i32_f32_sdwa v159, v153 dst_sel:BYTE_1 dst_unused:UNUSED_PRESERVE src0_sel:DWORD
	v_cvt_rpi_i32_f32_sdwa v156, v142 dst_sel:BYTE_2 dst_unused:UNUSED_PRESERVE src0_sel:DWORD
	v_cvt_rpi_i32_f32_sdwa v157, v146 dst_sel:BYTE_2 dst_unused:UNUSED_PRESERVE src0_sel:DWORD
	v_cvt_rpi_i32_f32_sdwa v158, v150 dst_sel:BYTE_2 dst_unused:UNUSED_PRESERVE src0_sel:DWORD
	v_cvt_rpi_i32_f32_sdwa v159, v154 dst_sel:BYTE_2 dst_unused:UNUSED_PRESERVE src0_sel:DWORD
	v_cvt_rpi_i32_f32_sdwa v156, v143 dst_sel:BYTE_3 dst_unused:UNUSED_PRESERVE src0_sel:DWORD
	v_cvt_rpi_i32_f32_sdwa v157, v147 dst_sel:BYTE_3 dst_unused:UNUSED_PRESERVE src0_sel:DWORD
	v_cvt_rpi_i32_f32_sdwa v158, v151 dst_sel:BYTE_3 dst_unused:UNUSED_PRESERVE src0_sel:DWORD
	v_cvt_rpi_i32_f32_sdwa v159, v155 dst_sel:BYTE_3 dst_unused:UNUSED_PRESERVE src0_sel:DWORD
	s_nop 0
	global_store_dwordx2 v[136:137], v[156:157], off
	global_store_dwordx2 v[136:137], v[158:159], off offset:128
	s_nop 1
	s_waitcnt lgkmcnt(0)
	v_mov_b32_e32 v160, v161
	ds_read_b32 v161, v205 offset:192
	v_mul_f32_e32 v160, 0xbfb8aa3b, v160
	v_mul_f32_e32 v140, v160, v96
	v_mul_f32_e32 v141, v160, v97
	v_mul_f32_e32 v142, v160, v98
	v_mul_f32_e32 v143, v160, v99
	v_mul_f32_e32 v144, v160, v92
	v_mul_f32_e32 v145, v160, v93
	v_mul_f32_e32 v146, v160, v94
	v_mul_f32_e32 v147, v160, v95
	v_mul_f32_e32 v148, v160, v88
	v_mul_f32_e32 v149, v160, v89
	v_mul_f32_e32 v150, v160, v90
	v_mul_f32_e32 v151, v160, v91
	v_mul_f32_e32 v152, v160, v84
	v_mul_f32_e32 v153, v160, v85
	v_mul_f32_e32 v154, v160, v86
	v_mul_f32_e32 v155, v160, v87
	v_exp_f32_e32 v140, v140
	v_exp_f32_e32 v141, v141
	v_exp_f32_e32 v142, v142
	v_exp_f32_e32 v143, v143
	v_exp_f32_e32 v144, v144
	v_exp_f32_e32 v145, v145
	v_exp_f32_e32 v146, v146
	v_exp_f32_e32 v147, v147
	v_exp_f32_e32 v148, v148
	v_exp_f32_e32 v149, v149
	v_exp_f32_e32 v150, v150
	v_exp_f32_e32 v151, v151
	v_exp_f32_e32 v152, v152
	v_exp_f32_e32 v153, v153
	v_exp_f32_e32 v154, v154
	v_exp_f32_e32 v155, v155
	v_fma_f32 v140, v140, s8, s8
	v_fma_f32 v141, v141, s8, s8
	v_fma_f32 v142, v142, s8, s8
	v_fma_f32 v143, v143, s8, s8
	v_fma_f32 v144, v144, s8, s8
	v_fma_f32 v145, v145, s8, s8
	v_fma_f32 v146, v146, s8, s8
	v_fma_f32 v147, v147, s8, s8
	v_fma_f32 v148, v148, s8, s8
	v_fma_f32 v149, v149, s8, s8
	v_fma_f32 v150, v150, s8, s8
	v_fma_f32 v151, v151, s8, s8
	v_fma_f32 v152, v152, s8, s8
	v_fma_f32 v153, v153, s8, s8
	v_fma_f32 v154, v154, s8, s8
	v_fma_f32 v155, v155, s8, s8
	v_rcp_f32_e32 v140, v140
	v_rcp_f32_e32 v141, v141
	v_rcp_f32_e32 v142, v142
	v_rcp_f32_e32 v143, v143
	v_rcp_f32_e32 v144, v144
	v_rcp_f32_e32 v145, v145
	v_rcp_f32_e32 v146, v146
	v_rcp_f32_e32 v147, v147
	v_rcp_f32_e32 v148, v148
	v_rcp_f32_e32 v149, v149
	v_rcp_f32_e32 v150, v150
	v_rcp_f32_e32 v151, v151
	v_rcp_f32_e32 v152, v152
	v_rcp_f32_e32 v153, v153
	v_rcp_f32_e32 v154, v154
	v_rcp_f32_e32 v155, v155
	s_mov_b64 s[0:1], 0x8000
	v_lshl_add_u64 v[136:137], v[134:135], 0, s[0:1]
	v_cvt_rpi_i32_f32_sdwa v156, v140 dst_sel:BYTE_0 dst_unused:UNUSED_PAD src0_sel:DWORD
	v_cvt_rpi_i32_f32_sdwa v157, v144 dst_sel:BYTE_0 dst_unused:UNUSED_PAD src0_sel:DWORD
	v_cvt_rpi_i32_f32_sdwa v158, v148 dst_sel:BYTE_0 dst_unused:UNUSED_PAD src0_sel:DWORD
	v_cvt_rpi_i32_f32_sdwa v159, v152 dst_sel:BYTE_0 dst_unused:UNUSED_PAD src0_sel:DWORD
	v_cvt_rpi_i32_f32_sdwa v156, v141 dst_sel:BYTE_1 dst_unused:UNUSED_PRESERVE src0_sel:DWORD
	v_cvt_rpi_i32_f32_sdwa v157, v145 dst_sel:BYTE_1 dst_unused:UNUSED_PRESERVE src0_sel:DWORD
	v_cvt_rpi_i32_f32_sdwa v158, v149 dst_sel:BYTE_1 dst_unused:UNUSED_PRESERVE src0_sel:DWORD
	v_cvt_rpi_i32_f32_sdwa v159, v153 dst_sel:BYTE_1 dst_unused:UNUSED_PRESERVE src0_sel:DWORD
	v_cvt_rpi_i32_f32_sdwa v156, v142 dst_sel:BYTE_2 dst_unused:UNUSED_PRESERVE src0_sel:DWORD
	v_cvt_rpi_i32_f32_sdwa v157, v146 dst_sel:BYTE_2 dst_unused:UNUSED_PRESERVE src0_sel:DWORD
	v_cvt_rpi_i32_f32_sdwa v158, v150 dst_sel:BYTE_2 dst_unused:UNUSED_PRESERVE src0_sel:DWORD
	v_cvt_rpi_i32_f32_sdwa v159, v154 dst_sel:BYTE_2 dst_unused:UNUSED_PRESERVE src0_sel:DWORD
	v_cvt_rpi_i32_f32_sdwa v156, v143 dst_sel:BYTE_3 dst_unused:UNUSED_PRESERVE src0_sel:DWORD
	v_cvt_rpi_i32_f32_sdwa v157, v147 dst_sel:BYTE_3 dst_unused:UNUSED_PRESERVE src0_sel:DWORD
	v_cvt_rpi_i32_f32_sdwa v158, v151 dst_sel:BYTE_3 dst_unused:UNUSED_PRESERVE src0_sel:DWORD
	v_cvt_rpi_i32_f32_sdwa v159, v155 dst_sel:BYTE_3 dst_unused:UNUSED_PRESERVE src0_sel:DWORD
	s_nop 0
	global_store_dwordx2 v[136:137], v[156:157], off
	global_store_dwordx2 v[136:137], v[158:159], off offset:128
	s_nop 1
	s_waitcnt lgkmcnt(0)
;     __device__ __forceinline__ void operator()(const f32x4 (&acc)[2][2][4][2], const Unit& u, int wr, int wc, int fr, int fq) const {
;     ...
;                 unsigned char* gb8 = wsb + (pn < 14 ? WS_GA : WS_GB) + ((pn - 10) & 3) * 256 + cl;
; #pragma unroll
;                 for (int ai = 0; ai < 2; ++ai)
; #pragma unroll
;                     for (int m = 0; m < 4; ++m) { unsigned char* rowp = gb8 + (size_t)(row0 + ai * HALF + m * 16) * 1024; const float nrf = -1.4426950408889634f * rsr[ai * HALF + m * 16];
; #pragma unroll
;                         for (int bj = 0; bj < 2; ++bj) { u32x2 w; w.x = 0u; w.y = 0u;
; #pragma unroll
;                             for (int e = 0; e < 4; ++e) { const float x0 = acc[ai][bj][m][0][e], x1 = acc[ai][bj][m][1][e];
;                                 const float r0 = 255.0f * __builtin_amdgcn_rcpf(1.0f + __builtin_amdgcn_exp2f(nrf * x0)), r1 = 255.0f * __builtin_amdgcn_rcpf(1.0f + __builtin_amdgcn_exp2f(nrf * x1));
;                                 w.x |= (unsigned)(r0 + 0.5f) << (8 * e); w.y |= (unsigned)(r1 + 0.5f) << (8 * e); }
;                             *(u32x2*)(rowp + bj * HALF) = w; }
;                         asm volatile("" ::: "memory"); }
	v_mov_b32_e32 v160, v161
	ds_read_b32 v161, v205 offset:512
	v_mul_f32_e32 v160, 0xbfb8aa3b, v160
	v_mul_f32_e32 v140, v160, v80
	v_mul_f32_e32 v141, v160, v81
	v_mul_f32_e32 v142, v160, v82
	v_mul_f32_e32 v143, v160, v83
	v_mul_f32_e32 v144, v160, v76
	v_mul_f32_e32 v145, v160, v77
	v_mul_f32_e32 v146, v160, v78
	v_mul_f32_e32 v147, v160, v79
	v_mul_f32_e32 v148, v160, v72
	v_mul_f32_e32 v149, v160, v73
	v_mul_f32_e32 v150, v160, v74
	v_mul_f32_e32 v151, v160, v75
	v_mul_f32_e32 v152, v160, v68
	v_mul_f32_e32 v153, v160, v69
	v_mul_f32_e32 v154, v160, v70
	v_mul_f32_e32 v155, v160, v71
	v_exp_f32_e32 v140, v140
	v_exp_f32_e32 v141, v141
	v_exp_f32_e32 v142, v142
	v_exp_f32_e32 v143, v143
	v_exp_f32_e32 v144, v144
	v_exp_f32_e32 v145, v145
	v_exp_f32_e32 v146, v146
	v_exp_f32_e32 v147, v147
	v_exp_f32_e32 v148, v148
	v_exp_f32_e32 v149, v149
	v_exp_f32_e32 v150, v150
	v_exp_f32_e32 v151, v151
	v_exp_f32_e32 v152, v152
	v_exp_f32_e32 v153, v153
	v_exp_f32_e32 v154, v154
	v_exp_f32_e32 v155, v155
	v_fma_f32 v140, v140, s8, s8
	v_fma_f32 v141, v141, s8, s8
	v_fma_f32 v142, v142, s8, s8
	v_fma_f32 v143, v143, s8, s8
	v_fma_f32 v144, v144, s8, s8
	v_fma_f32 v145, v145, s8, s8
	v_fma_f32 v146, v146, s8, s8
	v_fma_f32 v147, v147, s8, s8
	v_fma_f32 v148, v148, s8, s8
	v_fma_f32 v149, v149, s8, s8
	v_fma_f32 v150, v150, s8, s8
	v_fma_f32 v151, v151, s8, s8
	v_fma_f32 v152, v152, s8, s8
	v_fma_f32 v153, v153, s8, s8
	v_fma_f32 v154, v154, s8, s8
	v_fma_f32 v155, v155, s8, s8
	v_rcp_f32_e32 v140, v140
	v_rcp_f32_e32 v141, v141
	v_rcp_f32_e32 v142, v142
	v_rcp_f32_e32 v143, v143
	v_rcp_f32_e32 v144, v144
	v_rcp_f32_e32 v145, v145
	v_rcp_f32_e32 v146, v146
	v_rcp_f32_e32 v147, v147
	v_rcp_f32_e32 v148, v148
	v_rcp_f32_e32 v149, v149
	v_rcp_f32_e32 v150, v150
	v_rcp_f32_e32 v151, v151
	v_rcp_f32_e32 v152, v152
	v_rcp_f32_e32 v153, v153
	v_rcp_f32_e32 v154, v154
	v_rcp_f32_e32 v155, v155
	s_mov_b64 s[0:1], 0xc000
	v_lshl_add_u64 v[136:137], v[134:135], 0, s[0:1]
	v_cvt_rpi_i32_f32_sdwa v156, v140 dst_sel:BYTE_0 dst_unused:UNUSED_PAD src0_sel:DWORD
	v_cvt_rpi_i32_f32_sdwa v157, v144 dst_sel:BYTE_0 dst_unused:UNUSED_PAD src0_sel:DWORD
	v_cvt_rpi_i32_f32_sdwa v158, v148 dst_sel:BYTE_0 dst_unused:UNUSED_PAD src0_sel:DWORD
	v_cvt_rpi_i32_f32_sdwa v159, v152 dst_sel:BYTE_0 dst_unused:UNUSED_PAD src0_sel:DWORD
	v_cvt_rpi_i32_f32_sdwa v156, v141 dst_sel:BYTE_1 dst_unused:UNUSED_PRESERVE src0_sel:DWORD
	v_cvt_rpi_i32_f32_sdwa v157, v145 dst_sel:BYTE_1 dst_unused:UNUSED_PRESERVE src0_sel:DWORD
	v_cvt_rpi_i32_f32_sdwa v158, v149 dst_sel:BYTE_1 dst_unused:UNUSED_PRESERVE src0_sel:DWORD
	v_cvt_rpi_i32_f32_sdwa v159, v153 dst_sel:BYTE_1 dst_unused:UNUSED_PRESERVE src0_sel:DWORD
	v_cvt_rpi_i32_f32_sdwa v156, v142 dst_sel:BYTE_2 dst_unused:UNUSED_PRESERVE src0_sel:DWORD
	v_cvt_rpi_i32_f32_sdwa v157, v146 dst_sel:BYTE_2 dst_unused:UNUSED_PRESERVE src0_sel:DWORD
	v_cvt_rpi_i32_f32_sdwa v158, v150 dst_sel:BYTE_2 dst_unused:UNUSED_PRESERVE src0_sel:DWORD
	v_cvt_rpi_i32_f32_sdwa v159, v154 dst_sel:BYTE_2 dst_unused:UNUSED_PRESERVE src0_sel:DWORD
	v_cvt_rpi_i32_f32_sdwa v156, v143 dst_sel:BYTE_3 dst_unused:UNUSED_PRESERVE src0_sel:DWORD
	v_cvt_rpi_i32_f32_sdwa v157, v147 dst_sel:BYTE_3 dst_unused:UNUSED_PRESERVE src0_sel:DWORD
	v_cvt_rpi_i32_f32_sdwa v158, v151 dst_sel:BYTE_3 dst_unused:UNUSED_PRESERVE src0_sel:DWORD
	v_cvt_rpi_i32_f32_sdwa v159, v155 dst_sel:BYTE_3 dst_unused:UNUSED_PRESERVE src0_sel:DWORD
	s_nop 0
	global_store_dwordx2 v[136:137], v[156:157], off
	global_store_dwordx2 v[136:137], v[158:159], off offset:128
	s_nop 1
	s_waitcnt lgkmcnt(0)
	v_mov_b32_e32 v160, v161
	ds_read_b32 v161, v205 offset:576
	v_mul_f32_e32 v160, 0xbfb8aa3b, v160
	v_mul_f32_e32 v140, v160, v64
	v_mul_f32_e32 v141, v160, v65
	v_mul_f32_e32 v142, v160, v66
	v_mul_f32_e32 v143, v160, v67
	v_mul_f32_e32 v144, v160, v60
	v_mul_f32_e32 v145, v160, v61
	v_mul_f32_e32 v146, v160, v62
	v_mul_f32_e32 v147, v160, v63
	v_mul_f32_e32 v148, v160, v56
	v_mul_f32_e32 v149, v160, v57
	v_mul_f32_e32 v150, v160, v58
	v_mul_f32_e32 v151, v160, v59
	v_mul_f32_e32 v152, v160, v52
	v_mul_f32_e32 v153, v160, v53
	v_mul_f32_e32 v154, v160, v54
	v_mul_f32_e32 v155, v160, v55
	v_exp_f32_e32 v140, v140
	v_exp_f32_e32 v141, v141
	v_exp_f32_e32 v142, v142
	v_exp_f32_e32 v143, v143
	v_exp_f32_e32 v144, v144
	v_exp_f32_e32 v145, v145
	v_exp_f32_e32 v146, v146
	v_exp_f32_e32 v147, v147
	v_exp_f32_e32 v148, v148
	v_exp_f32_e32 v149, v149
	v_exp_f32_e32 v150, v150
	v_exp_f32_e32 v151, v151
	v_exp_f32_e32 v152, v152
	v_exp_f32_e32 v153, v153
	v_exp_f32_e32 v154, v154
	v_exp_f32_e32 v155, v155
	v_fma_f32 v140, v140, s8, s8
	v_fma_f32 v141, v141, s8, s8
	v_fma_f32 v142, v142, s8, s8
	v_fma_f32 v143, v143, s8, s8
	v_fma_f32 v144, v144, s8, s8
	v_fma_f32 v145, v145, s8, s8
	v_fma_f32 v146, v146, s8, s8
	v_fma_f32 v147, v147, s8, s8
	v_fma_f32 v148, v148, s8, s8
	v_fma_f32 v149, v149, s8, s8
	v_fma_f32 v150, v150, s8, s8
	v_fma_f32 v151, v151, s8, s8
	v_fma_f32 v152, v152, s8, s8
	v_fma_f32 v153, v153, s8, s8
	v_fma_f32 v154, v154, s8, s8
	v_fma_f32 v155, v155, s8, s8
	v_rcp_f32_e32 v140, v140
	v_rcp_f32_e32 v141, v141
	v_rcp_f32_e32 v142, v142
	v_rcp_f32_e32 v143, v143
	v_rcp_f32_e32 v144, v144
	v_rcp_f32_e32 v145, v145
	v_rcp_f32_e32 v146, v146
	v_rcp_f32_e32 v147, v147
	v_rcp_f32_e32 v148, v148
	v_rcp_f32_e32 v149, v149
	v_rcp_f32_e32 v150, v150
	v_rcp_f32_e32 v151, v151
	v_rcp_f32_e32 v152, v152
	v_rcp_f32_e32 v153, v153
	v_rcp_f32_e32 v154, v154
	v_rcp_f32_e32 v155, v155
	s_mov_b64 s[0:1], 0x20000
	v_lshl_add_u64 v[136:137], v[134:135], 0, s[0:1]
	v_cvt_rpi_i32_f32_sdwa v156, v140 dst_sel:BYTE_0 dst_unused:UNUSED_PAD src0_sel:DWORD
;     __device__ __forceinline__ void operator()(const f32x4 (&acc)[2][2][4][2], const Unit& u, int wr, int wc, int fr, int fq) const {
;     ...
;                 unsigned char* gb8 = wsb + (pn < 14 ? WS_GA : WS_GB) + ((pn - 10) & 3) * 256 + cl;
; #pragma unroll
;                 for (int ai = 0; ai < 2; ++ai)
; #pragma unroll
;                     for (int m = 0; m < 4; ++m) { unsigned char* rowp = gb8 + (size_t)(row0 + ai * HALF + m * 16) * 1024; const float nrf = -1.4426950408889634f * rsr[ai * HALF + m * 16];
; #pragma unroll
;                         for (int bj = 0; bj < 2; ++bj) { u32x2 w; w.x = 0u; w.y = 0u;
; #pragma unroll
;                             for (int e = 0; e < 4; ++e) { const float x0 = acc[ai][bj][m][0][e], x1 = acc[ai][bj][m][1][e];
;                                 const float r0 = 255.0f * __builtin_amdgcn_rcpf(1.0f + __builtin_amdgcn_exp2f(nrf * x0)), r1 = 255.0f * __builtin_amdgcn_rcpf(1.0f + __builtin_amdgcn_exp2f(nrf * x1));
;                                 w.x |= (unsigned)(r0 + 0.5f) << (8 * e); w.y |= (unsigned)(r1 + 0.5f) << (8 * e); }
;                             *(u32x2*)(rowp + bj * HALF) = w; }
;                         asm volatile("" ::: "memory"); }
	v_cvt_rpi_i32_f32_sdwa v157, v144 dst_sel:BYTE_0 dst_unused:UNUSED_PAD src0_sel:DWORD
	v_cvt_rpi_i32_f32_sdwa v158, v148 dst_sel:BYTE_0 dst_unused:UNUSED_PAD src0_sel:DWORD
	v_cvt_rpi_i32_f32_sdwa v159, v152 dst_sel:BYTE_0 dst_unused:UNUSED_PAD src0_sel:DWORD
	v_cvt_rpi_i32_f32_sdwa v156, v141 dst_sel:BYTE_1 dst_unused:UNUSED_PRESERVE src0_sel:DWORD
	v_cvt_rpi_i32_f32_sdwa v157, v145 dst_sel:BYTE_1 dst_unused:UNUSED_PRESERVE src0_sel:DWORD
	v_cvt_rpi_i32_f32_sdwa v158, v149 dst_sel:BYTE_1 dst_unused:UNUSED_PRESERVE src0_sel:DWORD
	v_cvt_rpi_i32_f32_sdwa v159, v153 dst_sel:BYTE_1 dst_unused:UNUSED_PRESERVE src0_sel:DWORD
	v_cvt_rpi_i32_f32_sdwa v156, v142 dst_sel:BYTE_2 dst_unused:UNUSED_PRESERVE src0_sel:DWORD
	v_cvt_rpi_i32_f32_sdwa v157, v146 dst_sel:BYTE_2 dst_unused:UNUSED_PRESERVE src0_sel:DWORD
	v_cvt_rpi_i32_f32_sdwa v158, v150 dst_sel:BYTE_2 dst_unused:UNUSED_PRESERVE src0_sel:DWORD
	v_cvt_rpi_i32_f32_sdwa v159, v154 dst_sel:BYTE_2 dst_unused:UNUSED_PRESERVE src0_sel:DWORD
	v_cvt_rpi_i32_f32_sdwa v156, v143 dst_sel:BYTE_3 dst_unused:UNUSED_PRESERVE src0_sel:DWORD
	v_cvt_rpi_i32_f32_sdwa v157, v147 dst_sel:BYTE_3 dst_unused:UNUSED_PRESERVE src0_sel:DWORD
	v_cvt_rpi_i32_f32_sdwa v158, v151 dst_sel:BYTE_3 dst_unused:UNUSED_PRESERVE src0_sel:DWORD
	v_cvt_rpi_i32_f32_sdwa v159, v155 dst_sel:BYTE_3 dst_unused:UNUSED_PRESERVE src0_sel:DWORD
	s_nop 0
	global_store_dwordx2 v[136:137], v[156:157], off
	global_store_dwordx2 v[136:137], v[158:159], off offset:128
	s_nop 1
	s_waitcnt lgkmcnt(0)
	v_mov_b32_e32 v160, v161
	ds_read_b32 v161, v205 offset:640
	v_mul_f32_e32 v160, 0xbfb8aa3b, v160
	v_mul_f32_e32 v140, v160, v48
	v_mul_f32_e32 v141, v160, v49
	v_mul_f32_e32 v142, v160, v50
	v_mul_f32_e32 v143, v160, v51
	v_mul_f32_e32 v144, v160, v44
	v_mul_f32_e32 v145, v160, v45
	v_mul_f32_e32 v146, v160, v46
	v_mul_f32_e32 v147, v160, v47
	v_mul_f32_e32 v148, v160, v40
	v_mul_f32_e32 v149, v160, v41
	v_mul_f32_e32 v150, v160, v42
	v_mul_f32_e32 v151, v160, v43
	v_mul_f32_e32 v152, v160, v36
	v_mul_f32_e32 v153, v160, v37
	v_mul_f32_e32 v154, v160, v38
	v_mul_f32_e32 v155, v160, v39
	v_exp_f32_e32 v140, v140
	v_exp_f32_e32 v141, v141
	v_exp_f32_e32 v142, v142
	v_exp_f32_e32 v143, v143
	v_exp_f32_e32 v144, v144
	v_exp_f32_e32 v145, v145
	v_exp_f32_e32 v146, v146
	v_exp_f32_e32 v147, v147
	v_exp_f32_e32 v148, v148
	v_exp_f32_e32 v149, v149
	v_exp_f32_e32 v150, v150
	v_exp_f32_e32 v151, v151
	v_exp_f32_e32 v152, v152
	v_exp_f32_e32 v153, v153
	v_exp_f32_e32 v154, v154
	v_exp_f32_e32 v155, v155
	v_fma_f32 v140, v140, s8, s8
	v_fma_f32 v141, v141, s8, s8
	v_fma_f32 v142, v142, s8, s8
	v_fma_f32 v143, v143, s8, s8
	v_fma_f32 v144, v144, s8, s8
	v_fma_f32 v145, v145, s8, s8
	v_fma_f32 v146, v146, s8, s8
	v_fma_f32 v147, v147, s8, s8
	v_fma_f32 v148, v148, s8, s8
	v_fma_f32 v149, v149, s8, s8
	v_fma_f32 v150, v150, s8, s8
	v_fma_f32 v151, v151, s8, s8
	v_fma_f32 v152, v152, s8, s8
	v_fma_f32 v153, v153, s8, s8
	v_fma_f32 v154, v154, s8, s8
	v_fma_f32 v155, v155, s8, s8
	v_rcp_f32_e32 v140, v140
	v_rcp_f32_e32 v141, v141
	v_rcp_f32_e32 v142, v142
	v_rcp_f32_e32 v143, v143
	v_rcp_f32_e32 v144, v144
	v_rcp_f32_e32 v145, v145
	v_rcp_f32_e32 v146, v146
	v_rcp_f32_e32 v147, v147
	v_rcp_f32_e32 v148, v148
	v_rcp_f32_e32 v149, v149
	v_rcp_f32_e32 v150, v150
	v_rcp_f32_e32 v151, v151
	v_rcp_f32_e32 v152, v152
	v_rcp_f32_e32 v153, v153
	v_rcp_f32_e32 v154, v154
	v_rcp_f32_e32 v155, v155
	s_mov_b64 s[0:1], 0x24000
	v_lshl_add_u64 v[136:137], v[134:135], 0, s[0:1]
	v_cvt_rpi_i32_f32_sdwa v156, v140 dst_sel:BYTE_0 dst_unused:UNUSED_PAD src0_sel:DWORD
	v_cvt_rpi_i32_f32_sdwa v157, v144 dst_sel:BYTE_0 dst_unused:UNUSED_PAD src0_sel:DWORD
	v_cvt_rpi_i32_f32_sdwa v158, v148 dst_sel:BYTE_0 dst_unused:UNUSED_PAD src0_sel:DWORD
	v_cvt_rpi_i32_f32_sdwa v159, v152 dst_sel:BYTE_0 dst_unused:UNUSED_PAD src0_sel:DWORD
	v_cvt_rpi_i32_f32_sdwa v156, v141 dst_sel:BYTE_1 dst_unused:UNUSED_PRESERVE src0_sel:DWORD
	v_cvt_rpi_i32_f32_sdwa v157, v145 dst_sel:BYTE_1 dst_unused:UNUSED_PRESERVE src0_sel:DWORD
	v_cvt_rpi_i32_f32_sdwa v158, v149 dst_sel:BYTE_1 dst_unused:UNUSED_PRESERVE src0_sel:DWORD
	v_cvt_rpi_i32_f32_sdwa v159, v153 dst_sel:BYTE_1 dst_unused:UNUSED_PRESERVE src0_sel:DWORD
	v_cvt_rpi_i32_f32_sdwa v156, v142 dst_sel:BYTE_2 dst_unused:UNUSED_PRESERVE src0_sel:DWORD
	v_cvt_rpi_i32_f32_sdwa v157, v146 dst_sel:BYTE_2 dst_unused:UNUSED_PRESERVE src0_sel:DWORD
	v_cvt_rpi_i32_f32_sdwa v158, v150 dst_sel:BYTE_2 dst_unused:UNUSED_PRESERVE src0_sel:DWORD
	v_cvt_rpi_i32_f32_sdwa v159, v154 dst_sel:BYTE_2 dst_unused:UNUSED_PRESERVE src0_sel:DWORD
	v_cvt_rpi_i32_f32_sdwa v156, v143 dst_sel:BYTE_3 dst_unused:UNUSED_PRESERVE src0_sel:DWORD
	v_cvt_rpi_i32_f32_sdwa v157, v147 dst_sel:BYTE_3 dst_unused:UNUSED_PRESERVE src0_sel:DWORD
	v_cvt_rpi_i32_f32_sdwa v158, v151 dst_sel:BYTE_3 dst_unused:UNUSED_PRESERVE src0_sel:DWORD
	v_cvt_rpi_i32_f32_sdwa v159, v155 dst_sel:BYTE_3 dst_unused:UNUSED_PRESERVE src0_sel:DWORD
	s_nop 0
	global_store_dwordx2 v[136:137], v[156:157], off
	global_store_dwordx2 v[136:137], v[158:159], off offset:128
	s_nop 1
	s_waitcnt lgkmcnt(0)
;     __device__ __forceinline__ void operator()(const f32x4 (&acc)[2][2][4][2], const Unit& u, int wr, int wc, int fr, int fq) const {
;     ...
;                 unsigned char* gb8 = wsb + (pn < 14 ? WS_GA : WS_GB) + ((pn - 10) & 3) * 256 + cl;
; #pragma unroll
;                 for (int ai = 0; ai < 2; ++ai)
; #pragma unroll
;                     for (int m = 0; m < 4; ++m) { unsigned char* rowp = gb8 + (size_t)(row0 + ai * HALF + m * 16) * 1024; const float nrf = -1.4426950408889634f * rsr[ai * HALF + m * 16];
; #pragma unroll
;                         for (int bj = 0; bj < 2; ++bj) { u32x2 w; w.x = 0u; w.y = 0u;
; #pragma unroll
;                             for (int e = 0; e < 4; ++e) { const float x0 = acc[ai][bj][m][0][e], x1 = acc[ai][bj][m][1][e];
;                                 const float r0 = 255.0f * __builtin_amdgcn_rcpf(1.0f + __builtin_amdgcn_exp2f(nrf * x0)), r1 = 255.0f * __builtin_amdgcn_rcpf(1.0f + __builtin_amdgcn_exp2f(nrf * x1));
;                                 w.x |= (unsigned)(r0 + 0.5f) << (8 * e); w.y |= (unsigned)(r1 + 0.5f) << (8 * e); }
;                             *(u32x2*)(rowp + bj * HALF) = w; }
;                         asm volatile("" ::: "memory"); }
	v_mov_b32_e32 v160, v161
	ds_read_b32 v161, v205 offset:704
	v_mul_f32_e32 v160, 0xbfb8aa3b, v160
	v_mul_f32_e32 v140, v160, v32
	v_mul_f32_e32 v141, v160, v33
	v_mul_f32_e32 v142, v160, v34
	v_mul_f32_e32 v143, v160, v35
	v_mul_f32_e32 v144, v160, v28
	v_mul_f32_e32 v145, v160, v29
	v_mul_f32_e32 v146, v160, v30
	v_mul_f32_e32 v147, v160, v31
	v_mul_f32_e32 v148, v160, v24
	v_mul_f32_e32 v149, v160, v25
	v_mul_f32_e32 v150, v160, v26
	v_mul_f32_e32 v151, v160, v27
	v_mul_f32_e32 v152, v160, v20
	v_mul_f32_e32 v153, v160, v21
	v_mul_f32_e32 v154, v160, v22
	v_mul_f32_e32 v155, v160, v23
	v_exp_f32_e32 v140, v140
	v_exp_f32_e32 v141, v141
	v_exp_f32_e32 v142, v142
	v_exp_f32_e32 v143, v143
	v_exp_f32_e32 v144, v144
	v_exp_f32_e32 v145, v145
	v_exp_f32_e32 v146, v146
	v_exp_f32_e32 v147, v147
	v_exp_f32_e32 v148, v148
	v_exp_f32_e32 v149, v149
	v_exp_f32_e32 v150, v150
	v_exp_f32_e32 v151, v151
	v_exp_f32_e32 v152, v152
	v_exp_f32_e32 v153, v153
	v_exp_f32_e32 v154, v154
	v_exp_f32_e32 v155, v155
	v_fma_f32 v140, v140, s8, s8
	v_fma_f32 v141, v141, s8, s8
	v_fma_f32 v142, v142, s8, s8
	v_fma_f32 v143, v143, s8, s8
	v_fma_f32 v144, v144, s8, s8
	v_fma_f32 v145, v145, s8, s8
	v_fma_f32 v146, v146, s8, s8
	v_fma_f32 v147, v147, s8, s8
	v_fma_f32 v148, v148, s8, s8
	v_fma_f32 v149, v149, s8, s8
	v_fma_f32 v150, v150, s8, s8
	v_fma_f32 v151, v151, s8, s8
	v_fma_f32 v152, v152, s8, s8
	v_fma_f32 v153, v153, s8, s8
	v_fma_f32 v154, v154, s8, s8
	v_fma_f32 v155, v155, s8, s8
	v_rcp_f32_e32 v140, v140
	v_rcp_f32_e32 v141, v141
	v_rcp_f32_e32 v142, v142
	v_rcp_f32_e32 v143, v143
	v_rcp_f32_e32 v144, v144
	v_rcp_f32_e32 v145, v145
	v_rcp_f32_e32 v146, v146
	v_rcp_f32_e32 v147, v147
	v_rcp_f32_e32 v148, v148
	v_rcp_f32_e32 v149, v149
	v_rcp_f32_e32 v150, v150
	v_rcp_f32_e32 v151, v151
	v_rcp_f32_e32 v152, v152
	v_rcp_f32_e32 v153, v153
	v_rcp_f32_e32 v154, v154
	v_rcp_f32_e32 v155, v155
	s_mov_b64 s[0:1], 0x28000
	v_lshl_add_u64 v[136:137], v[134:135], 0, s[0:1]
	v_cvt_rpi_i32_f32_sdwa v156, v140 dst_sel:BYTE_0 dst_unused:UNUSED_PAD src0_sel:DWORD
	v_cvt_rpi_i32_f32_sdwa v157, v144 dst_sel:BYTE_0 dst_unused:UNUSED_PAD src0_sel:DWORD
	v_cvt_rpi_i32_f32_sdwa v158, v148 dst_sel:BYTE_0 dst_unused:UNUSED_PAD src0_sel:DWORD
	v_cvt_rpi_i32_f32_sdwa v159, v152 dst_sel:BYTE_0 dst_unused:UNUSED_PAD src0_sel:DWORD
	v_cvt_rpi_i32_f32_sdwa v156, v141 dst_sel:BYTE_1 dst_unused:UNUSED_PRESERVE src0_sel:DWORD
	v_cvt_rpi_i32_f32_sdwa v157, v145 dst_sel:BYTE_1 dst_unused:UNUSED_PRESERVE src0_sel:DWORD
	v_cvt_rpi_i32_f32_sdwa v158, v149 dst_sel:BYTE_1 dst_unused:UNUSED_PRESERVE src0_sel:DWORD
	v_cvt_rpi_i32_f32_sdwa v159, v153 dst_sel:BYTE_1 dst_unused:UNUSED_PRESERVE src0_sel:DWORD
	v_cvt_rpi_i32_f32_sdwa v156, v142 dst_sel:BYTE_2 dst_unused:UNUSED_PRESERVE src0_sel:DWORD
	v_cvt_rpi_i32_f32_sdwa v157, v146 dst_sel:BYTE_2 dst_unused:UNUSED_PRESERVE src0_sel:DWORD
	v_cvt_rpi_i32_f32_sdwa v158, v150 dst_sel:BYTE_2 dst_unused:UNUSED_PRESERVE src0_sel:DWORD
	v_cvt_rpi_i32_f32_sdwa v159, v154 dst_sel:BYTE_2 dst_unused:UNUSED_PRESERVE src0_sel:DWORD
	v_cvt_rpi_i32_f32_sdwa v156, v143 dst_sel:BYTE_3 dst_unused:UNUSED_PRESERVE src0_sel:DWORD
	v_cvt_rpi_i32_f32_sdwa v157, v147 dst_sel:BYTE_3 dst_unused:UNUSED_PRESERVE src0_sel:DWORD
	v_cvt_rpi_i32_f32_sdwa v158, v151 dst_sel:BYTE_3 dst_unused:UNUSED_PRESERVE src0_sel:DWORD
	v_cvt_rpi_i32_f32_sdwa v159, v155 dst_sel:BYTE_3 dst_unused:UNUSED_PRESERVE src0_sel:DWORD
	s_nop 0
	global_store_dwordx2 v[136:137], v[156:157], off
	global_store_dwordx2 v[136:137], v[158:159], off offset:128
	s_nop 1
	s_waitcnt lgkmcnt(0)
;     __device__ __forceinline__ void operator()(const f32x4 (&acc)[2][2][4][2], const Unit& u, int wr, int wc, int fr, int fq) const {
;     ...
;                 unsigned char* gb8 = wsb + (pn < 14 ? WS_GA : WS_GB) + ((pn - 10) & 3) * 256 + cl;
; #pragma unroll
;                 for (int ai = 0; ai < 2; ++ai)
; #pragma unroll
;                     for (int m = 0; m < 4; ++m) { unsigned char* rowp = gb8 + (size_t)(row0 + ai * HALF + m * 16) * 1024; const float nrf = -1.4426950408889634f * rsr[ai * HALF + m * 16];
; #pragma unroll
;                         for (int bj = 0; bj < 2; ++bj) { u32x2 w; w.x = 0u; w.y = 0u;
; #pragma unroll
;                             for (int e = 0; e < 4; ++e) { const float x0 = acc[ai][bj][m][0][e], x1 = acc[ai][bj][m][1][e];
;                                 const float r0 = 255.0f * __builtin_amdgcn_rcpf(1.0f + __builtin_amdgcn_exp2f(nrf * x0)), r1 = 255.0f * __builtin_amdgcn_rcpf(1.0f + __builtin_amdgcn_exp2f(nrf * x1));
;                                 w.x |= (unsigned)(r0 + 0.5f) << (8 * e); w.y |= (unsigned)(r1 + 0.5f) << (8 * e); }
;                             *(u32x2*)(rowp + bj * HALF) = w; }
;                         asm volatile("" ::: "memory"); }
	v_mov_b32_e32 v160, v161
	v_mul_f32_e32 v160, 0xbfb8aa3b, v160
	v_mul_f32_e32 v140, v160, v16
	v_mul_f32_e32 v141, v160, v17
	v_mul_f32_e32 v142, v160, v18
	v_mul_f32_e32 v143, v160, v19
	v_mul_f32_e32 v144, v160, v12
	v_mul_f32_e32 v145, v160, v13
	v_mul_f32_e32 v146, v160, v14
	v_mul_f32_e32 v147, v160, v15
	v_mul_f32_e32 v148, v160, v8
	v_mul_f32_e32 v149, v160, v9
	v_mul_f32_e32 v150, v160, v10
	v_mul_f32_e32 v151, v160, v11
	v_mul_f32_e32 v152, v160, v4
	v_mul_f32_e32 v153, v160, v5
	v_mul_f32_e32 v154, v160, v6
	v_mul_f32_e32 v155, v160, v7
	v_exp_f32_e32 v140, v140
	v_exp_f32_e32 v141, v141
	v_exp_f32_e32 v142, v142
	v_exp_f32_e32 v143, v143
	v_exp_f32_e32 v144, v144
	v_exp_f32_e32 v145, v145
	v_exp_f32_e32 v146, v146
	v_exp_f32_e32 v147, v147
	v_exp_f32_e32 v148, v148
	v_exp_f32_e32 v149, v149
	v_exp_f32_e32 v150, v150
	v_exp_f32_e32 v151, v151
	v_exp_f32_e32 v152, v152
	v_exp_f32_e32 v153, v153
	v_exp_f32_e32 v154, v154
	v_exp_f32_e32 v155, v155
	v_fma_f32 v140, v140, s8, s8
	v_fma_f32 v141, v141, s8, s8
	v_fma_f32 v142, v142, s8, s8
	v_fma_f32 v143, v143, s8, s8
	v_fma_f32 v144, v144, s8, s8
	v_fma_f32 v145, v145, s8, s8
	v_fma_f32 v146, v146, s8, s8
	v_fma_f32 v147, v147, s8, s8
	v_fma_f32 v148, v148, s8, s8
	v_fma_f32 v149, v149, s8, s8
	v_fma_f32 v150, v150, s8, s8
	v_fma_f32 v151, v151, s8, s8
	v_fma_f32 v152, v152, s8, s8
	v_fma_f32 v153, v153, s8, s8
	v_fma_f32 v154, v154, s8, s8
	v_fma_f32 v155, v155, s8, s8
	v_rcp_f32_e32 v140, v140
	v_rcp_f32_e32 v141, v141
	v_rcp_f32_e32 v142, v142
	v_rcp_f32_e32 v143, v143
	v_rcp_f32_e32 v144, v144
	v_rcp_f32_e32 v145, v145
	v_rcp_f32_e32 v146, v146
	v_rcp_f32_e32 v147, v147
	v_rcp_f32_e32 v148, v148
	v_rcp_f32_e32 v149, v149
	v_rcp_f32_e32 v150, v150
	v_rcp_f32_e32 v151, v151
	v_rcp_f32_e32 v152, v152
	v_rcp_f32_e32 v153, v153
	v_rcp_f32_e32 v154, v154
	v_rcp_f32_e32 v155, v155
	s_mov_b64 s[0:1], 0x2c000
	v_lshl_add_u64 v[136:137], v[134:135], 0, s[0:1]
	v_cvt_rpi_i32_f32_sdwa v156, v140 dst_sel:BYTE_0 dst_unused:UNUSED_PAD src0_sel:DWORD
	v_cvt_rpi_i32_f32_sdwa v157, v144 dst_sel:BYTE_0 dst_unused:UNUSED_PAD src0_sel:DWORD
	v_cvt_rpi_i32_f32_sdwa v158, v148 dst_sel:BYTE_0 dst_unused:UNUSED_PAD src0_sel:DWORD
	v_cvt_rpi_i32_f32_sdwa v159, v152 dst_sel:BYTE_0 dst_unused:UNUSED_PAD src0_sel:DWORD
	v_cvt_rpi_i32_f32_sdwa v156, v141 dst_sel:BYTE_1 dst_unused:UNUSED_PRESERVE src0_sel:DWORD
	v_cvt_rpi_i32_f32_sdwa v157, v145 dst_sel:BYTE_1 dst_unused:UNUSED_PRESERVE src0_sel:DWORD
	v_cvt_rpi_i32_f32_sdwa v158, v149 dst_sel:BYTE_1 dst_unused:UNUSED_PRESERVE src0_sel:DWORD
	v_cvt_rpi_i32_f32_sdwa v159, v153 dst_sel:BYTE_1 dst_unused:UNUSED_PRESERVE src0_sel:DWORD
	v_cvt_rpi_i32_f32_sdwa v156, v142 dst_sel:BYTE_2 dst_unused:UNUSED_PRESERVE src0_sel:DWORD
	v_cvt_rpi_i32_f32_sdwa v157, v146 dst_sel:BYTE_2 dst_unused:UNUSED_PRESERVE src0_sel:DWORD
	v_cvt_rpi_i32_f32_sdwa v158, v150 dst_sel:BYTE_2 dst_unused:UNUSED_PRESERVE src0_sel:DWORD
	v_cvt_rpi_i32_f32_sdwa v159, v154 dst_sel:BYTE_2 dst_unused:UNUSED_PRESERVE src0_sel:DWORD
	v_cvt_rpi_i32_f32_sdwa v156, v143 dst_sel:BYTE_3 dst_unused:UNUSED_PRESERVE src0_sel:DWORD
	v_cvt_rpi_i32_f32_sdwa v157, v147 dst_sel:BYTE_3 dst_unused:UNUSED_PRESERVE src0_sel:DWORD
	v_cvt_rpi_i32_f32_sdwa v158, v151 dst_sel:BYTE_3 dst_unused:UNUSED_PRESERVE src0_sel:DWORD
	v_cvt_rpi_i32_f32_sdwa v159, v155 dst_sel:BYTE_3 dst_unused:UNUSED_PRESERVE src0_sel:DWORD
	s_nop 0
	global_store_dwordx2 v[136:137], v[156:157], off
	global_store_dwordx2 v[136:137], v[158:159], off offset:128
	s_nop 1
	s_mov_b64 s[0:1], 0
